# pair-wait with shifted parity (V fragment i paired with K fragment i+1)
# baseline (speedup 1.0000x reference)
.Lattn_pa0:
	s_waitcnt lgkmcnt(7)
	v_mfma_f32_16x16x32_bf16 v[64:67], v[160:163], v[96:99], 0
	v_exp_f32_e32 v88, v88
	v_mfma_f32_16x16x32_bf16 v[68:71], v[160:163], v[112:115], 0
	v_exp_f32_e32 v92, v92
	ds_read_b128 v[160:163], v201 offset:20480
	s_add_u32 s16, s22, s10
	s_addc_u32 s17, s23, s11
	s_add_u32 s15, s22, s12
	s_addc_u32 s14, s23, s13
	s_add_u32 s8, s16, 0x3bc00200
	s_addc_u32 s9, s17, 0
	s_add_u32 s6, s15, 0x23a50000
	s_addc_u32 s7, s14, 0
	s_waitcnt lgkmcnt(6)
	v_mfma_f32_16x16x32_bf16 v[0:3], v[164:167], v[216:219], v[0:3]
	v_cvt_pk_bf16_f32 v242, v80, v81
	v_mfma_f32_16x16x32_bf16 v[4:7], v[164:167], v[238:241], v[4:7]
	v_exp_f32_e32 v89, v89
	ds_read_b128 v[164:167], v209 offset:8192
	s_waitcnt vmcnt(4)
	ds_write_b128 v225, v[152:155] offset:49152
	v_mfma_f32_16x16x32_bf16 v[68:71], v[168:171], v[116:119], v[68:71]
	v_exp_f32_e32 v93, v93
	v_mfma_f32_16x16x32_bf16 v[64:67], v[168:171], v[100:103], v[64:67]
	v_cvt_pk_bf16_f32 v243, v82, v83
	ds_read_b128 v[168:171], v202 offset:20480
	ds_write_b128 v226, v[156:159] offset:49152
	s_waitcnt lgkmcnt(8)
	v_mfma_f32_16x16x32_bf16 v[12:15], v[172:175], v[238:241], v[12:15]
	v_exp_f32_e32 v90, v90
	v_mfma_f32_16x16x32_bf16 v[8:11], v[172:175], v[216:219], v[8:11]
	v_exp_f32_e32 v94, v94
	ds_read_b128 v[172:175], v209 offset:10240
	ds_write_b64 v227, v[132:133] offset:32768
	v_mfma_f32_16x16x32_bf16 v[64:67], v[176:179], v[104:107], v[64:67]
	v_cvt_pk_bf16_f32 v204, v84, v85
	v_mfma_f32_16x16x32_bf16 v[68:71], v[176:179], v[120:123], v[68:71]
	v_exp_f32_e32 v91, v91
	ds_read_b128 v[176:179], v203 offset:20480
	ds_write_b64 v228, v[134:135] offset:32768
	s_waitcnt lgkmcnt(10)
	v_mfma_f32_16x16x32_bf16 v[16:19], v[180:183], v[216:219], v[16:19]
	v_exp_f32_e32 v95, v95
	v_mfma_f32_16x16x32_bf16 v[20:23], v[180:183], v[238:241], v[20:23]
	v_cvt_pk_bf16_f32 v205, v86, v87
	v_add_f32_e32 v220, v220, v88
	ds_read_b128 v[180:183], v209 offset:12288
	ds_write_b64 v229, v[128:129] offset:32768
	v_mfma_f32_16x16x32_bf16 v[68:71], v[230:233], v[124:127], v[68:71]
	v_add_f32_e32 v221, v221, v92
	v_add_f32_e32 v220, v220, v89
	v_mfma_f32_16x16x32_bf16 v[64:67], v[230:233], v[108:111], v[64:67]
	v_add_f32_e32 v221, v221, v93
	v_cvt_pk_bf16_f32 v244, v88, v89
	ds_read_b128 v[230:233], v246 offset:20480
	ds_write_b64 v184, v[130:131] offset:32768
	s_waitcnt lgkmcnt(12)
	v_mfma_f32_16x16x32_bf16 v[28:31], v[234:237], v[238:241], v[28:31]
	v_cvt_pk_bf16_f32 v245, v90, v91
	v_cvt_pk_bf16_f32 v206, v92, v93
	v_mfma_f32_16x16x32_bf16 v[24:27], v[234:237], v[216:219], v[24:27]
	v_cvt_pk_bf16_f32 v207, v94, v95
	ds_read_b128 v[234:237], v209 offset:14336
	global_load_dwordx4 v[132:135], v198, s[8:9]
	v_mfma_f32_16x16x32_bf16 v[72:75], v[160:163], v[96:99], 0
	v_add_f32_e32 v220, v220, v90
	v_add_f32_e32 v221, v221, v94
	v_mfma_f32_16x16x32_bf16 v[76:79], v[160:163], v[112:115], 0
	v_add_f32_e32 v220, v220, v91
	v_add_f32_e32 v221, v221, v95
	ds_read_b128 v[160:163], v201 offset:24576
	global_load_dwordx4 v[128:131], v199, s[8:9]
	s_waitcnt lgkmcnt(11)
	v_mfma_f32_16x16x32_bf16 v[32:35], v[164:167], v[216:219], v[32:35]
	v_add_f32_e32 v194, v194, v220
	v_add_f32_e32 v195, v195, v221
	v_mfma_f32_16x16x32_bf16 v[36:39], v[164:167], v[238:241], v[36:39]
	v_exp_f32_e32 v64, v64
	ds_read_b128 v[164:167], v210 offset:0
	global_load_dwordx4 v[152:155], v196, s[6:7]
	v_mfma_f32_16x16x32_bf16 v[76:79], v[168:171], v[116:119], v[76:79]
	v_exp_f32_e32 v68, v68
	v_mfma_f32_16x16x32_bf16 v[72:75], v[168:171], v[100:103], v[72:75]
	v_exp_f32_e32 v65, v65
	ds_read_b128 v[168:171], v202 offset:24576
	global_load_dwordx4 v[156:159], v197, s[6:7]
	s_waitcnt lgkmcnt(9)
	v_mfma_f32_16x16x32_bf16 v[44:47], v[172:175], v[238:241], v[44:47]
	v_exp_f32_e32 v69, v69
	v_mfma_f32_16x16x32_bf16 v[40:43], v[172:175], v[216:219], v[40:43]
	v_exp_f32_e32 v66, v66
	ds_read_b128 v[172:175], v210 offset:2048
	v_mfma_f32_16x16x32_bf16 v[72:75], v[176:179], v[104:107], v[72:75]
	v_exp_f32_e32 v70, v70
	v_mfma_f32_16x16x32_bf16 v[76:79], v[176:179], v[120:123], v[76:79]
	v_exp_f32_e32 v67, v67
	ds_read_b128 v[176:179], v203 offset:24576
	s_waitcnt lgkmcnt(7)
	v_mfma_f32_16x16x32_bf16 v[48:51], v[180:183], v[216:219], v[48:51]
	v_exp_f32_e32 v71, v71
	v_mfma_f32_16x16x32_bf16 v[52:55], v[180:183], v[238:241], v[52:55]
	v_add_f32_e32 v220, v64, v65
	ds_read_b128 v[180:183], v210 offset:4096
	v_mfma_f32_16x16x32_bf16 v[76:79], v[230:233], v[124:127], v[76:79]
	v_add_f32_e32 v221, v68, v69
	v_mfma_f32_16x16x32_bf16 v[72:75], v[230:233], v[108:111], v[72:75]
	v_add_f32_e32 v220, v220, v66
	ds_read_b128 v[230:233], v246 offset:24576
	s_waitcnt lgkmcnt(6)
	v_mfma_f32_16x16x32_bf16 v[60:63], v[234:237], v[238:241], v[60:63]
	v_add_f32_e32 v221, v221, v70
	v_add_f32_e32 v220, v220, v67
	v_mfma_f32_16x16x32_bf16 v[56:59], v[234:237], v[216:219], v[56:59]
	v_add_f32_e32 v221, v221, v71
	ds_read_b128 v[234:237], v210 offset:6144
	v_mfma_f32_16x16x32_bf16 v[80:83], v[160:163], v[96:99], 0
	v_exp_f32_e32 v72, v72
	v_mfma_f32_16x16x32_bf16 v[84:87], v[160:163], v[112:115], 0
	v_exp_f32_e32 v76, v76
	ds_read_b128 v[160:163], v201 offset:28672
	s_waitcnt lgkmcnt(6)
	v_mfma_f32_16x16x32_bf16 v[0:3], v[164:167], v[242:245], v[0:3]
	v_exp_f32_e32 v73, v73
	v_mfma_f32_16x16x32_bf16 v[4:7], v[164:167], v[204:207], v[4:7]
	v_exp_f32_e32 v77, v77
	ds_read_b128 v[164:167], v210 offset:8192
	v_mfma_f32_16x16x32_bf16 v[84:87], v[168:171], v[116:119], v[84:87]
	v_exp_f32_e32 v74, v74
	v_mfma_f32_16x16x32_bf16 v[80:83], v[168:171], v[100:103], v[80:83]
	v_exp_f32_e32 v78, v78
	ds_read_b128 v[168:171], v202 offset:28672
	s_waitcnt lgkmcnt(6)
	v_mfma_f32_16x16x32_bf16 v[12:15], v[172:175], v[204:207], v[12:15]
	v_exp_f32_e32 v75, v75
	v_mfma_f32_16x16x32_bf16 v[8:11], v[172:175], v[242:245], v[8:11]
	v_exp_f32_e32 v79, v79
	ds_read_b128 v[172:175], v210 offset:10240
	v_mfma_f32_16x16x32_bf16 v[80:83], v[176:179], v[104:107], v[80:83]
	v_add_f32_e32 v220, v220, v72
	v_add_f32_e32 v221, v221, v76
	v_mfma_f32_16x16x32_bf16 v[84:87], v[176:179], v[120:123], v[84:87]
	v_add_f32_e32 v220, v220, v73
	ds_read_b128 v[176:179], v203 offset:28672
	s_waitcnt lgkmcnt(6)
	v_mfma_f32_16x16x32_bf16 v[16:19], v[180:183], v[242:245], v[16:19]
	v_add_f32_e32 v221, v221, v77
	v_add_f32_e32 v220, v220, v74
	v_mfma_f32_16x16x32_bf16 v[20:23], v[180:183], v[204:207], v[20:23]
	v_add_f32_e32 v221, v221, v78
	ds_read_b128 v[180:183], v210 offset:12288
	v_mfma_f32_16x16x32_bf16 v[84:87], v[230:233], v[124:127], v[84:87]
	v_add_f32_e32 v220, v220, v75
	v_add_f32_e32 v221, v221, v79
	v_mfma_f32_16x16x32_bf16 v[80:83], v[230:233], v[108:111], v[80:83]
	v_cvt_pk_bf16_f32 v216, v64, v65
	ds_read_b128 v[230:233], v246 offset:28672
	s_waitcnt lgkmcnt(6)
	v_mfma_f32_16x16x32_bf16 v[28:31], v[234:237], v[204:207], v[28:31]
	v_cvt_pk_bf16_f32 v217, v66, v67
	v_cvt_pk_bf16_f32 v238, v68, v69
	v_mfma_f32_16x16x32_bf16 v[24:27], v[234:237], v[242:245], v[24:27]
	v_cvt_pk_bf16_f32 v239, v70, v71
	ds_read_b128 v[234:237], v210 offset:14336
	v_mfma_f32_16x16x32_bf16 v[88:91], v[160:163], v[96:99], 0
	v_exp_f32_e32 v80, v80
	v_mfma_f32_16x16x32_bf16 v[92:95], v[160:163], v[112:115], 0
	v_exp_f32_e32 v84, v84
	ds_read_b128 v[160:163], v201 offset:32768
	s_waitcnt lgkmcnt(6)
	v_mfma_f32_16x16x32_bf16 v[32:35], v[164:167], v[242:245], v[32:35]
	v_exp_f32_e32 v81, v81
	v_mfma_f32_16x16x32_bf16 v[36:39], v[164:167], v[204:207], v[36:39]
	v_exp_f32_e32 v85, v85
	ds_read_b128 v[164:167], v209 offset:16384
	v_mfma_f32_16x16x32_bf16 v[92:95], v[168:171], v[116:119], v[92:95]
	v_exp_f32_e32 v82, v82
	v_mfma_f32_16x16x32_bf16 v[88:91], v[168:171], v[100:103], v[88:91]
	v_exp_f32_e32 v86, v86
	ds_read_b128 v[168:171], v202 offset:32768
	s_waitcnt lgkmcnt(6)
	v_mfma_f32_16x16x32_bf16 v[44:47], v[172:175], v[204:207], v[44:47]
	v_exp_f32_e32 v83, v83
	v_mfma_f32_16x16x32_bf16 v[40:43], v[172:175], v[242:245], v[40:43]
	v_exp_f32_e32 v87, v87
	ds_read_b128 v[172:175], v209 offset:18432
	v_mfma_f32_16x16x32_bf16 v[88:91], v[176:179], v[104:107], v[88:91]
	v_add_f32_e32 v220, v220, v80
	v_add_f32_e32 v221, v221, v84
	v_mfma_f32_16x16x32_bf16 v[92:95], v[176:179], v[120:123], v[92:95]
	v_add_f32_e32 v220, v220, v81
	ds_read_b128 v[176:179], v203 offset:32768
	s_waitcnt lgkmcnt(6)
	v_mfma_f32_16x16x32_bf16 v[48:51], v[180:183], v[242:245], v[48:51]
	v_add_f32_e32 v221, v221, v85
	v_add_f32_e32 v220, v220, v82
	v_mfma_f32_16x16x32_bf16 v[52:55], v[180:183], v[204:207], v[52:55]
	v_add_f32_e32 v221, v221, v86
	ds_read_b128 v[180:183], v209 offset:20480
	v_mfma_f32_16x16x32_bf16 v[92:95], v[230:233], v[124:127], v[92:95]
	v_add_f32_e32 v220, v220, v83
	v_add_f32_e32 v221, v221, v87
	v_mfma_f32_16x16x32_bf16 v[88:91], v[230:233], v[108:111], v[88:91]
	v_cvt_pk_bf16_f32 v218, v72, v73
	ds_read_b128 v[230:233], v246 offset:32768
	s_waitcnt lgkmcnt(6)
	v_mfma_f32_16x16x32_bf16 v[60:63], v[234:237], v[204:207], v[60:63]
	v_cvt_pk_bf16_f32 v219, v74, v75
	v_cvt_pk_bf16_f32 v240, v76, v77
	v_mfma_f32_16x16x32_bf16 v[56:59], v[234:237], v[242:245], v[56:59]
	v_cvt_pk_bf16_f32 v241, v78, v79
	ds_read_b128 v[234:237], v209 offset:22528
	s_setprio 0
	v_mfma_f32_16x16x32_bf16 v[64:67], v[160:163], v[96:99], 0
	v_exp_f32_e32 v88, v88
	v_mfma_f32_16x16x32_bf16 v[68:71], v[160:163], v[112:115], 0
	v_exp_f32_e32 v92, v92
	ds_read_b128 v[160:163], v201 offset:36864
	s_add_u32 s8, s16, 0x3bc00280
	s_addc_u32 s9, s17, 0
	s_add_u32 s6, s15, 0x23a60000
	s_addc_u32 s7, s14, 0
	s_waitcnt lgkmcnt(6)
	v_mfma_f32_16x16x32_bf16 v[0:3], v[164:167], v[216:219], v[0:3]
	v_cvt_pk_bf16_f32 v242, v80, v81
	v_mfma_f32_16x16x32_bf16 v[4:7], v[164:167], v[238:241], v[4:7]
	v_exp_f32_e32 v89, v89
	ds_read_b128 v[164:167], v209 offset:24576
	s_waitcnt vmcnt(4)
	ds_write_b128 v225, v[136:139] offset:0
	v_mfma_f32_16x16x32_bf16 v[68:71], v[168:171], v[116:119], v[68:71]
	v_exp_f32_e32 v93, v93
	v_mfma_f32_16x16x32_bf16 v[64:67], v[168:171], v[100:103], v[64:67]
	v_cvt_pk_bf16_f32 v243, v82, v83
	ds_read_b128 v[168:171], v202 offset:36864
	ds_write_b128 v226, v[140:143] offset:0
	s_waitcnt lgkmcnt(8)
	v_mfma_f32_16x16x32_bf16 v[12:15], v[172:175], v[238:241], v[12:15]
	v_exp_f32_e32 v90, v90
	v_mfma_f32_16x16x32_bf16 v[8:11], v[172:175], v[216:219], v[8:11]
	v_exp_f32_e32 v94, v94
	ds_read_b128 v[172:175], v209 offset:26624
	ds_write_b64 v227, v[148:149] offset:49152
	v_mfma_f32_16x16x32_bf16 v[64:67], v[176:179], v[104:107], v[64:67]
	v_cvt_pk_bf16_f32 v204, v84, v85
	v_mfma_f32_16x16x32_bf16 v[68:71], v[176:179], v[120:123], v[68:71]
	v_exp_f32_e32 v91, v91
	ds_read_b128 v[176:179], v203 offset:36864
	ds_write_b64 v228, v[150:151] offset:49152
	s_waitcnt lgkmcnt(10)
	v_mfma_f32_16x16x32_bf16 v[16:19], v[180:183], v[216:219], v[16:19]
	v_exp_f32_e32 v95, v95
	v_mfma_f32_16x16x32_bf16 v[20:23], v[180:183], v[238:241], v[20:23]
	v_cvt_pk_bf16_f32 v205, v86, v87
	v_add_f32_e32 v220, v220, v88
	ds_read_b128 v[180:183], v209 offset:28672
	ds_write_b64 v229, v[144:145] offset:49152
	v_mfma_f32_16x16x32_bf16 v[68:71], v[230:233], v[124:127], v[68:71]
	v_add_f32_e32 v221, v221, v92
	v_add_f32_e32 v220, v220, v89
	v_mfma_f32_16x16x32_bf16 v[64:67], v[230:233], v[108:111], v[64:67]
	v_add_f32_e32 v221, v221, v93
	v_cvt_pk_bf16_f32 v244, v88, v89
	ds_read_b128 v[230:233], v246 offset:36864
	ds_write_b64 v184, v[146:147] offset:49152
	s_waitcnt lgkmcnt(12)
	v_mfma_f32_16x16x32_bf16 v[28:31], v[234:237], v[238:241], v[28:31]
	v_cvt_pk_bf16_f32 v245, v90, v91
	v_cvt_pk_bf16_f32 v206, v92, v93
	v_mfma_f32_16x16x32_bf16 v[24:27], v[234:237], v[216:219], v[24:27]
	v_cvt_pk_bf16_f32 v207, v94, v95
	ds_read_b128 v[234:237], v209 offset:30720
	global_load_dwordx4 v[148:151], v198, s[8:9]
	v_mfma_f32_16x16x32_bf16 v[72:75], v[160:163], v[96:99], 0
	v_add_f32_e32 v220, v220, v90
	v_add_f32_e32 v221, v221, v94
	v_mfma_f32_16x16x32_bf16 v[76:79], v[160:163], v[112:115], 0
	v_add_f32_e32 v220, v220, v91
	v_add_f32_e32 v221, v221, v95
	ds_read_b128 v[160:163], v201 offset:40960
	global_load_dwordx4 v[144:147], v199, s[8:9]
	s_waitcnt lgkmcnt(11)
	v_mfma_f32_16x16x32_bf16 v[32:35], v[164:167], v[216:219], v[32:35]
	v_add_f32_e32 v194, v194, v220
	v_add_f32_e32 v195, v195, v221
	v_mfma_f32_16x16x32_bf16 v[36:39], v[164:167], v[238:241], v[36:39]
	v_exp_f32_e32 v64, v64
	ds_read_b128 v[164:167], v210 offset:16384
	global_load_dwordx4 v[136:139], v196, s[6:7]
	v_mfma_f32_16x16x32_bf16 v[76:79], v[168:171], v[116:119], v[76:79]
	v_exp_f32_e32 v68, v68
	v_mfma_f32_16x16x32_bf16 v[72:75], v[168:171], v[100:103], v[72:75]
	v_exp_f32_e32 v65, v65
	ds_read_b128 v[168:171], v202 offset:40960
	global_load_dwordx4 v[140:143], v197, s[6:7]
	s_waitcnt lgkmcnt(9)
	v_mfma_f32_16x16x32_bf16 v[44:47], v[172:175], v[238:241], v[44:47]
	v_exp_f32_e32 v69, v69
	v_mfma_f32_16x16x32_bf16 v[40:43], v[172:175], v[216:219], v[40:43]
	v_exp_f32_e32 v66, v66
	ds_read_b128 v[172:175], v210 offset:18432
	v_mfma_f32_16x16x32_bf16 v[72:75], v[176:179], v[104:107], v[72:75]
	v_exp_f32_e32 v70, v70
	v_mfma_f32_16x16x32_bf16 v[76:79], v[176:179], v[120:123], v[76:79]
	v_exp_f32_e32 v67, v67
	ds_read_b128 v[176:179], v203 offset:40960
	s_waitcnt lgkmcnt(7)
	v_mfma_f32_16x16x32_bf16 v[48:51], v[180:183], v[216:219], v[48:51]
	v_exp_f32_e32 v71, v71
	v_mfma_f32_16x16x32_bf16 v[52:55], v[180:183], v[238:241], v[52:55]
	v_add_f32_e32 v220, v64, v65
	ds_read_b128 v[180:183], v210 offset:20480
	v_mfma_f32_16x16x32_bf16 v[76:79], v[230:233], v[124:127], v[76:79]
	v_add_f32_e32 v221, v68, v69
	v_mfma_f32_16x16x32_bf16 v[72:75], v[230:233], v[108:111], v[72:75]
	v_add_f32_e32 v220, v220, v66
	ds_read_b128 v[230:233], v246 offset:40960
	s_waitcnt lgkmcnt(6)
	v_mfma_f32_16x16x32_bf16 v[60:63], v[234:237], v[238:241], v[60:63]
	v_add_f32_e32 v221, v221, v70
	v_add_f32_e32 v220, v220, v67
	v_mfma_f32_16x16x32_bf16 v[56:59], v[234:237], v[216:219], v[56:59]
	v_add_f32_e32 v221, v221, v71
	ds_read_b128 v[234:237], v210 offset:22528
	v_mfma_f32_16x16x32_bf16 v[80:83], v[160:163], v[96:99], 0
	v_exp_f32_e32 v72, v72
	v_mfma_f32_16x16x32_bf16 v[84:87], v[160:163], v[112:115], 0
	v_exp_f32_e32 v76, v76
	ds_read_b128 v[160:163], v201 offset:45056
	s_waitcnt lgkmcnt(6)
	v_mfma_f32_16x16x32_bf16 v[0:3], v[164:167], v[242:245], v[0:3]
	v_exp_f32_e32 v73, v73
	v_mfma_f32_16x16x32_bf16 v[4:7], v[164:167], v[204:207], v[4:7]
	v_exp_f32_e32 v77, v77
	ds_read_b128 v[164:167], v210 offset:24576
	v_mfma_f32_16x16x32_bf16 v[84:87], v[168:171], v[116:119], v[84:87]
	v_exp_f32_e32 v74, v74
	v_mfma_f32_16x16x32_bf16 v[80:83], v[168:171], v[100:103], v[80:83]
	v_exp_f32_e32 v78, v78
	ds_read_b128 v[168:171], v202 offset:45056
	s_waitcnt lgkmcnt(6)
	v_mfma_f32_16x16x32_bf16 v[12:15], v[172:175], v[204:207], v[12:15]
	v_exp_f32_e32 v75, v75
	v_mfma_f32_16x16x32_bf16 v[8:11], v[172:175], v[242:245], v[8:11]
	v_exp_f32_e32 v79, v79
	ds_read_b128 v[172:175], v210 offset:26624
	v_mfma_f32_16x16x32_bf16 v[80:83], v[176:179], v[104:107], v[80:83]
	v_add_f32_e32 v220, v220, v72
	v_add_f32_e32 v221, v221, v76
	v_mfma_f32_16x16x32_bf16 v[84:87], v[176:179], v[120:123], v[84:87]
	v_add_f32_e32 v220, v220, v73
	ds_read_b128 v[176:179], v203 offset:45056
	s_waitcnt lgkmcnt(6)
	v_mfma_f32_16x16x32_bf16 v[16:19], v[180:183], v[242:245], v[16:19]
	v_add_f32_e32 v221, v221, v77
	v_add_f32_e32 v220, v220, v74
	v_mfma_f32_16x16x32_bf16 v[20:23], v[180:183], v[204:207], v[20:23]
	v_add_f32_e32 v221, v221, v78
	ds_read_b128 v[180:183], v210 offset:28672
	v_mfma_f32_16x16x32_bf16 v[84:87], v[230:233], v[124:127], v[84:87]
	v_add_f32_e32 v220, v220, v75
	v_add_f32_e32 v221, v221, v79
	v_mfma_f32_16x16x32_bf16 v[80:83], v[230:233], v[108:111], v[80:83]
	v_cvt_pk_bf16_f32 v216, v64, v65
	ds_read_b128 v[230:233], v246 offset:45056
	s_waitcnt lgkmcnt(6)
	v_mfma_f32_16x16x32_bf16 v[28:31], v[234:237], v[204:207], v[28:31]
	v_cvt_pk_bf16_f32 v217, v66, v67
	v_cvt_pk_bf16_f32 v238, v68, v69
	v_mfma_f32_16x16x32_bf16 v[24:27], v[234:237], v[242:245], v[24:27]
	v_cvt_pk_bf16_f32 v239, v70, v71
	ds_read_b128 v[234:237], v210 offset:30720
	v_mfma_f32_16x16x32_bf16 v[88:91], v[160:163], v[96:99], 0
	v_exp_f32_e32 v80, v80
	v_mfma_f32_16x16x32_bf16 v[92:95], v[160:163], v[112:115], 0
	v_exp_f32_e32 v84, v84
	s_waitcnt lgkmcnt(5)
	v_mfma_f32_16x16x32_bf16 v[32:35], v[164:167], v[242:245], v[32:35]
	v_exp_f32_e32 v81, v81
	v_mfma_f32_16x16x32_bf16 v[36:39], v[164:167], v[204:207], v[36:39]
	v_exp_f32_e32 v85, v85
	v_mfma_f32_16x16x32_bf16 v[92:95], v[168:171], v[116:119], v[92:95]
	v_exp_f32_e32 v82, v82
	v_mfma_f32_16x16x32_bf16 v[88:91], v[168:171], v[100:103], v[88:91]
	v_exp_f32_e32 v86, v86
	s_waitcnt lgkmcnt(3)
	v_mfma_f32_16x16x32_bf16 v[44:47], v[172:175], v[204:207], v[44:47]
	v_exp_f32_e32 v83, v83
	v_mfma_f32_16x16x32_bf16 v[40:43], v[172:175], v[242:245], v[40:43]
	v_exp_f32_e32 v87, v87
	v_mfma_f32_16x16x32_bf16 v[88:91], v[176:179], v[104:107], v[88:91]
	v_add_f32_e32 v220, v220, v80
	v_add_f32_e32 v221, v221, v84
	v_mfma_f32_16x16x32_bf16 v[92:95], v[176:179], v[120:123], v[92:95]
	v_add_f32_e32 v220, v220, v81
	s_waitcnt lgkmcnt(0)
	s_barrier
	ds_read_b128 v[160:163], v201 offset:49152
	ds_read_b128 v[164:167], v209 offset:32768
	ds_read_b128 v[168:171], v202 offset:49152
	ds_read_b128 v[172:175], v209 offset:34816
	ds_read_b128 v[176:179], v203 offset:49152
	v_mfma_f32_16x16x32_bf16 v[48:51], v[180:183], v[242:245], v[48:51]
	v_add_f32_e32 v221, v221, v85
	v_add_f32_e32 v220, v220, v82
	v_mfma_f32_16x16x32_bf16 v[52:55], v[180:183], v[204:207], v[52:55]
	v_add_f32_e32 v221, v221, v86
	ds_read_b128 v[180:183], v209 offset:36864
	v_mfma_f32_16x16x32_bf16 v[92:95], v[230:233], v[124:127], v[92:95]
	v_add_f32_e32 v220, v220, v83
	v_add_f32_e32 v221, v221, v87
	v_mfma_f32_16x16x32_bf16 v[88:91], v[230:233], v[108:111], v[88:91]
	v_cvt_pk_bf16_f32 v218, v72, v73
	ds_read_b128 v[230:233], v246 offset:49152
	s_waitcnt lgkmcnt(6)
	v_mfma_f32_16x16x32_bf16 v[60:63], v[234:237], v[204:207], v[60:63]
	v_cvt_pk_bf16_f32 v219, v74, v75
	v_cvt_pk_bf16_f32 v240, v76, v77
	v_mfma_f32_16x16x32_bf16 v[56:59], v[234:237], v[242:245], v[56:59]
	v_cvt_pk_bf16_f32 v241, v78, v79
	ds_read_b128 v[234:237], v209 offset:38912
	s_cmp_eq_u32 s100, 0
	s_cbranch_scc1 .Lattn_pa2
	s_setprio 1
.Lattn_pa2:
	v_mfma_f32_16x16x32_bf16 v[64:67], v[160:163], v[96:99], 0
	v_exp_f32_e32 v88, v88
	v_mfma_f32_16x16x32_bf16 v[68:71], v[160:163], v[112:115], 0
	v_exp_f32_e32 v92, v92
	ds_read_b128 v[160:163], v201 offset:53248
	s_add_u32 s8, s16, 0x3bc00300
	s_addc_u32 s9, s17, 0
	s_add_u32 s6, s15, 0x23a70000
	s_addc_u32 s7, s14, 0
	s_waitcnt lgkmcnt(6)
	v_mfma_f32_16x16x32_bf16 v[0:3], v[164:167], v[216:219], v[0:3]
	v_cvt_pk_bf16_f32 v242, v80, v81
	v_mfma_f32_16x16x32_bf16 v[4:7], v[164:167], v[238:241], v[4:7]
	v_exp_f32_e32 v89, v89
	ds_read_b128 v[164:167], v209 offset:40960
	s_waitcnt vmcnt(4)
	ds_write_b128 v225, v[152:155] offset:16384
	v_mfma_f32_16x16x32_bf16 v[68:71], v[168:171], v[116:119], v[68:71]
	v_exp_f32_e32 v93, v93
	v_mfma_f32_16x16x32_bf16 v[64:67], v[168:171], v[100:103], v[64:67]
	v_cvt_pk_bf16_f32 v243, v82, v83
	ds_read_b128 v[168:171], v202 offset:53248
	ds_write_b128 v226, v[156:159] offset:16384
	s_waitcnt lgkmcnt(8)
	v_mfma_f32_16x16x32_bf16 v[12:15], v[172:175], v[238:241], v[12:15]
	v_exp_f32_e32 v90, v90
	v_mfma_f32_16x16x32_bf16 v[8:11], v[172:175], v[216:219], v[8:11]
	v_exp_f32_e32 v94, v94
	ds_read_b128 v[172:175], v209 offset:43008
	ds_write_b64 v227, v[132:133] offset:0
	v_mfma_f32_16x16x32_bf16 v[64:67], v[176:179], v[104:107], v[64:67]
	v_cvt_pk_bf16_f32 v204, v84, v85
	v_mfma_f32_16x16x32_bf16 v[68:71], v[176:179], v[120:123], v[68:71]
	v_exp_f32_e32 v91, v91
	ds_read_b128 v[176:179], v203 offset:53248
	ds_write_b64 v228, v[134:135] offset:0
	s_waitcnt lgkmcnt(10)
	v_mfma_f32_16x16x32_bf16 v[16:19], v[180:183], v[216:219], v[16:19]
	v_exp_f32_e32 v95, v95
	v_mfma_f32_16x16x32_bf16 v[20:23], v[180:183], v[238:241], v[20:23]
	v_cvt_pk_bf16_f32 v205, v86, v87
	v_add_f32_e32 v220, v220, v88
	ds_read_b128 v[180:183], v209 offset:45056
	ds_write_b64 v229, v[128:129] offset:0
	v_mfma_f32_16x16x32_bf16 v[68:71], v[230:233], v[124:127], v[68:71]
	v_add_f32_e32 v221, v221, v92
	v_add_f32_e32 v220, v220, v89
	v_mfma_f32_16x16x32_bf16 v[64:67], v[230:233], v[108:111], v[64:67]
	v_add_f32_e32 v221, v221, v93
	v_cvt_pk_bf16_f32 v244, v88, v89
	ds_read_b128 v[230:233], v246 offset:53248
	ds_write_b64 v184, v[130:131] offset:0
	s_waitcnt lgkmcnt(12)
	v_mfma_f32_16x16x32_bf16 v[28:31], v[234:237], v[238:241], v[28:31]
	v_cvt_pk_bf16_f32 v245, v90, v91
	v_cvt_pk_bf16_f32 v206, v92, v93
	v_mfma_f32_16x16x32_bf16 v[24:27], v[234:237], v[216:219], v[24:27]
	v_cvt_pk_bf16_f32 v207, v94, v95
	ds_read_b128 v[234:237], v209 offset:47104
	global_load_dwordx4 v[132:135], v198, s[8:9]
	v_mfma_f32_16x16x32_bf16 v[72:75], v[160:163], v[96:99], 0
	v_add_f32_e32 v220, v220, v90
	v_add_f32_e32 v221, v221, v94
	v_mfma_f32_16x16x32_bf16 v[76:79], v[160:163], v[112:115], 0
	v_add_f32_e32 v220, v220, v91
	v_add_f32_e32 v221, v221, v95
	ds_read_b128 v[160:163], v201 offset:57344
	global_load_dwordx4 v[128:131], v199, s[8:9]
	s_waitcnt lgkmcnt(11)
	v_mfma_f32_16x16x32_bf16 v[32:35], v[164:167], v[216:219], v[32:35]
	v_add_f32_e32 v194, v194, v220
	v_add_f32_e32 v195, v195, v221
	v_mfma_f32_16x16x32_bf16 v[36:39], v[164:167], v[238:241], v[36:39]
	v_exp_f32_e32 v64, v64
	ds_read_b128 v[164:167], v210 offset:32768
	global_load_dwordx4 v[152:155], v196, s[6:7]
	v_mfma_f32_16x16x32_bf16 v[76:79], v[168:171], v[116:119], v[76:79]
	v_exp_f32_e32 v68, v68
	v_mfma_f32_16x16x32_bf16 v[72:75], v[168:171], v[100:103], v[72:75]
	v_exp_f32_e32 v65, v65
	ds_read_b128 v[168:171], v202 offset:57344
	global_load_dwordx4 v[156:159], v197, s[6:7]
	s_waitcnt lgkmcnt(9)
	v_mfma_f32_16x16x32_bf16 v[44:47], v[172:175], v[238:241], v[44:47]
	v_exp_f32_e32 v69, v69
	v_mfma_f32_16x16x32_bf16 v[40:43], v[172:175], v[216:219], v[40:43]
	v_exp_f32_e32 v66, v66
	ds_read_b128 v[172:175], v210 offset:34816
	v_mfma_f32_16x16x32_bf16 v[72:75], v[176:179], v[104:107], v[72:75]
	v_exp_f32_e32 v70, v70
	v_mfma_f32_16x16x32_bf16 v[76:79], v[176:179], v[120:123], v[76:79]
	v_exp_f32_e32 v67, v67
	ds_read_b128 v[176:179], v203 offset:57344
	s_waitcnt lgkmcnt(7)
	v_mfma_f32_16x16x32_bf16 v[48:51], v[180:183], v[216:219], v[48:51]
	v_exp_f32_e32 v71, v71
	v_mfma_f32_16x16x32_bf16 v[52:55], v[180:183], v[238:241], v[52:55]
	v_add_f32_e32 v220, v64, v65
	ds_read_b128 v[180:183], v210 offset:36864
	v_mfma_f32_16x16x32_bf16 v[76:79], v[230:233], v[124:127], v[76:79]
	v_add_f32_e32 v221, v68, v69
	v_mfma_f32_16x16x32_bf16 v[72:75], v[230:233], v[108:111], v[72:75]
	v_add_f32_e32 v220, v220, v66
	ds_read_b128 v[230:233], v246 offset:57344
	s_waitcnt lgkmcnt(6)
	v_mfma_f32_16x16x32_bf16 v[60:63], v[234:237], v[238:241], v[60:63]
	v_add_f32_e32 v221, v221, v70
	v_add_f32_e32 v220, v220, v67
	v_mfma_f32_16x16x32_bf16 v[56:59], v[234:237], v[216:219], v[56:59]
	v_add_f32_e32 v221, v221, v71
	ds_read_b128 v[234:237], v210 offset:38912
	v_mfma_f32_16x16x32_bf16 v[80:83], v[160:163], v[96:99], 0
	v_exp_f32_e32 v72, v72
	v_mfma_f32_16x16x32_bf16 v[84:87], v[160:163], v[112:115], 0
	v_exp_f32_e32 v76, v76
	ds_read_b128 v[160:163], v201 offset:61440
	s_waitcnt lgkmcnt(6)
	v_mfma_f32_16x16x32_bf16 v[0:3], v[164:167], v[242:245], v[0:3]
	v_exp_f32_e32 v73, v73
	v_mfma_f32_16x16x32_bf16 v[4:7], v[164:167], v[204:207], v[4:7]
	v_exp_f32_e32 v77, v77
	ds_read_b128 v[164:167], v210 offset:40960
	v_mfma_f32_16x16x32_bf16 v[84:87], v[168:171], v[116:119], v[84:87]
	v_exp_f32_e32 v74, v74
	v_mfma_f32_16x16x32_bf16 v[80:83], v[168:171], v[100:103], v[80:83]
	v_exp_f32_e32 v78, v78
	ds_read_b128 v[168:171], v202 offset:61440
	s_waitcnt lgkmcnt(6)
	v_mfma_f32_16x16x32_bf16 v[12:15], v[172:175], v[204:207], v[12:15]
	v_exp_f32_e32 v75, v75
	v_mfma_f32_16x16x32_bf16 v[8:11], v[172:175], v[242:245], v[8:11]
	v_exp_f32_e32 v79, v79
	ds_read_b128 v[172:175], v210 offset:43008
	v_mfma_f32_16x16x32_bf16 v[80:83], v[176:179], v[104:107], v[80:83]
	v_add_f32_e32 v220, v220, v72
	v_add_f32_e32 v221, v221, v76
	v_mfma_f32_16x16x32_bf16 v[84:87], v[176:179], v[120:123], v[84:87]
	v_add_f32_e32 v220, v220, v73
	ds_read_b128 v[176:179], v203 offset:61440
	s_waitcnt lgkmcnt(6)
	v_mfma_f32_16x16x32_bf16 v[16:19], v[180:183], v[242:245], v[16:19]
	v_add_f32_e32 v221, v221, v77
	v_add_f32_e32 v220, v220, v74
	v_mfma_f32_16x16x32_bf16 v[20:23], v[180:183], v[204:207], v[20:23]
	v_add_f32_e32 v221, v221, v78
	ds_read_b128 v[180:183], v210 offset:45056
	v_mfma_f32_16x16x32_bf16 v[84:87], v[230:233], v[124:127], v[84:87]
	v_add_f32_e32 v220, v220, v75
	v_add_f32_e32 v221, v221, v79
	v_mfma_f32_16x16x32_bf16 v[80:83], v[230:233], v[108:111], v[80:83]
	v_cvt_pk_bf16_f32 v216, v64, v65
	ds_read_b128 v[230:233], v246 offset:61440
	s_waitcnt lgkmcnt(6)
	v_mfma_f32_16x16x32_bf16 v[28:31], v[234:237], v[204:207], v[28:31]
	v_cvt_pk_bf16_f32 v217, v66, v67
	v_cvt_pk_bf16_f32 v238, v68, v69
	v_mfma_f32_16x16x32_bf16 v[24:27], v[234:237], v[242:245], v[24:27]
	v_cvt_pk_bf16_f32 v239, v70, v71
	ds_read_b128 v[234:237], v210 offset:47104
	v_mfma_f32_16x16x32_bf16 v[88:91], v[160:163], v[96:99], 0
	v_exp_f32_e32 v80, v80
	v_mfma_f32_16x16x32_bf16 v[92:95], v[160:163], v[112:115], 0
	v_exp_f32_e32 v84, v84
	ds_read_b128 v[160:163], v201 offset:0
	s_waitcnt lgkmcnt(6)
	v_mfma_f32_16x16x32_bf16 v[32:35], v[164:167], v[242:245], v[32:35]
	v_exp_f32_e32 v81, v81
	v_mfma_f32_16x16x32_bf16 v[36:39], v[164:167], v[204:207], v[36:39]
	v_exp_f32_e32 v85, v85
	ds_read_b128 v[164:167], v209 offset:49152
	v_mfma_f32_16x16x32_bf16 v[92:95], v[168:171], v[116:119], v[92:95]
	v_exp_f32_e32 v82, v82
	v_mfma_f32_16x16x32_bf16 v[88:91], v[168:171], v[100:103], v[88:91]
	v_exp_f32_e32 v86, v86
	ds_read_b128 v[168:171], v202 offset:0
	s_waitcnt lgkmcnt(6)
	v_mfma_f32_16x16x32_bf16 v[44:47], v[172:175], v[204:207], v[44:47]
	v_exp_f32_e32 v83, v83
	v_mfma_f32_16x16x32_bf16 v[40:43], v[172:175], v[242:245], v[40:43]
	v_exp_f32_e32 v87, v87
	ds_read_b128 v[172:175], v209 offset:51200
	v_mfma_f32_16x16x32_bf16 v[88:91], v[176:179], v[104:107], v[88:91]
	v_add_f32_e32 v220, v220, v80
	v_add_f32_e32 v221, v221, v84
	v_mfma_f32_16x16x32_bf16 v[92:95], v[176:179], v[120:123], v[92:95]
	v_add_f32_e32 v220, v220, v81
	ds_read_b128 v[176:179], v203 offset:0
	s_waitcnt lgkmcnt(6)
	v_mfma_f32_16x16x32_bf16 v[48:51], v[180:183], v[242:245], v[48:51]
	v_add_f32_e32 v221, v221, v85
	v_add_f32_e32 v220, v220, v82
	v_mfma_f32_16x16x32_bf16 v[52:55], v[180:183], v[204:207], v[52:55]
	v_add_f32_e32 v221, v221, v86
	ds_read_b128 v[180:183], v209 offset:53248
	v_mfma_f32_16x16x32_bf16 v[92:95], v[230:233], v[124:127], v[92:95]
	v_add_f32_e32 v220, v220, v83
	v_add_f32_e32 v221, v221, v87
	v_mfma_f32_16x16x32_bf16 v[88:91], v[230:233], v[108:111], v[88:91]
	v_cvt_pk_bf16_f32 v218, v72, v73
	ds_read_b128 v[230:233], v246 offset:0
	s_waitcnt lgkmcnt(6)
	v_mfma_f32_16x16x32_bf16 v[60:63], v[234:237], v[204:207], v[60:63]
	v_cvt_pk_bf16_f32 v219, v74, v75
	v_cvt_pk_bf16_f32 v240, v76, v77
	v_mfma_f32_16x16x32_bf16 v[56:59], v[234:237], v[242:245], v[56:59]
	v_cvt_pk_bf16_f32 v241, v78, v79
	ds_read_b128 v[234:237], v209 offset:55296
	s_setprio 0
	v_mfma_f32_16x16x32_bf16 v[64:67], v[160:163], v[96:99], 0
	v_exp_f32_e32 v88, v88
	v_mfma_f32_16x16x32_bf16 v[68:71], v[160:163], v[112:115], 0
	v_exp_f32_e32 v92, v92
	ds_read_b128 v[160:163], v201 offset:4096
	s_add_u32 s8, s16, 0x3bc00380
	s_addc_u32 s9, s17, 0
	s_add_u32 s6, s15, 0x23a80000
	s_addc_u32 s7, s14, 0
	s_waitcnt lgkmcnt(6)
	v_mfma_f32_16x16x32_bf16 v[0:3], v[164:167], v[216:219], v[0:3]
	v_cvt_pk_bf16_f32 v242, v80, v81
	v_mfma_f32_16x16x32_bf16 v[4:7], v[164:167], v[238:241], v[4:7]
	v_exp_f32_e32 v89, v89
	ds_read_b128 v[164:167], v209 offset:57344
	s_waitcnt vmcnt(4)
	ds_write_b128 v225, v[136:139] offset:32768
	v_mfma_f32_16x16x32_bf16 v[68:71], v[168:171], v[116:119], v[68:71]
	v_exp_f32_e32 v93, v93
	v_mfma_f32_16x16x32_bf16 v[64:67], v[168:171], v[100:103], v[64:67]
	v_cvt_pk_bf16_f32 v243, v82, v83
	ds_read_b128 v[168:171], v202 offset:4096
	ds_write_b128 v226, v[140:143] offset:32768
	s_waitcnt lgkmcnt(8)
	v_mfma_f32_16x16x32_bf16 v[12:15], v[172:175], v[238:241], v[12:15]
	v_exp_f32_e32 v90, v90
	v_mfma_f32_16x16x32_bf16 v[8:11], v[172:175], v[216:219], v[8:11]
	v_exp_f32_e32 v94, v94
	ds_read_b128 v[172:175], v209 offset:59392
	ds_write_b64 v227, v[148:149] offset:16384
	v_mfma_f32_16x16x32_bf16 v[64:67], v[176:179], v[104:107], v[64:67]
	v_cvt_pk_bf16_f32 v204, v84, v85
	v_mfma_f32_16x16x32_bf16 v[68:71], v[176:179], v[120:123], v[68:71]
	v_exp_f32_e32 v91, v91
	ds_read_b128 v[176:179], v203 offset:4096
	ds_write_b64 v228, v[150:151] offset:16384
	s_waitcnt lgkmcnt(10)
	v_mfma_f32_16x16x32_bf16 v[16:19], v[180:183], v[216:219], v[16:19]
	v_exp_f32_e32 v95, v95
	v_mfma_f32_16x16x32_bf16 v[20:23], v[180:183], v[238:241], v[20:23]
	v_cvt_pk_bf16_f32 v205, v86, v87
	v_add_f32_e32 v220, v220, v88
	ds_read_b128 v[180:183], v209 offset:61440
	ds_write_b64 v229, v[144:145] offset:16384
	v_mfma_f32_16x16x32_bf16 v[68:71], v[230:233], v[124:127], v[68:71]
	v_add_f32_e32 v221, v221, v92
	v_add_f32_e32 v220, v220, v89
	v_mfma_f32_16x16x32_bf16 v[64:67], v[230:233], v[108:111], v[64:67]
	v_add_f32_e32 v221, v221, v93
	v_cvt_pk_bf16_f32 v244, v88, v89
	ds_read_b128 v[230:233], v246 offset:4096
	ds_write_b64 v184, v[146:147] offset:16384
	s_waitcnt lgkmcnt(12)
	v_mfma_f32_16x16x32_bf16 v[28:31], v[234:237], v[238:241], v[28:31]
	v_cvt_pk_bf16_f32 v245, v90, v91
	v_cvt_pk_bf16_f32 v206, v92, v93
	v_mfma_f32_16x16x32_bf16 v[24:27], v[234:237], v[216:219], v[24:27]
	v_cvt_pk_bf16_f32 v207, v94, v95
	ds_read_b128 v[234:237], v209 offset:63488
	global_load_dwordx4 v[148:151], v198, s[8:9]
	v_mfma_f32_16x16x32_bf16 v[72:75], v[160:163], v[96:99], 0
	v_add_f32_e32 v220, v220, v90
	v_add_f32_e32 v221, v221, v94
	v_mfma_f32_16x16x32_bf16 v[76:79], v[160:163], v[112:115], 0
	v_add_f32_e32 v220, v220, v91
	v_add_f32_e32 v221, v221, v95
	ds_read_b128 v[160:163], v201 offset:8192
	global_load_dwordx4 v[144:147], v199, s[8:9]
	s_waitcnt lgkmcnt(11)
	v_mfma_f32_16x16x32_bf16 v[32:35], v[164:167], v[216:219], v[32:35]
	v_add_f32_e32 v194, v194, v220
	v_add_f32_e32 v195, v195, v221
	v_mfma_f32_16x16x32_bf16 v[36:39], v[164:167], v[238:241], v[36:39]
	v_exp_f32_e32 v64, v64
	ds_read_b128 v[164:167], v210 offset:49152
	global_load_dwordx4 v[136:139], v196, s[6:7]
	v_mfma_f32_16x16x32_bf16 v[76:79], v[168:171], v[116:119], v[76:79]
	v_exp_f32_e32 v68, v68
	v_mfma_f32_16x16x32_bf16 v[72:75], v[168:171], v[100:103], v[72:75]
	v_exp_f32_e32 v65, v65
	ds_read_b128 v[168:171], v202 offset:8192
	global_load_dwordx4 v[140:143], v197, s[6:7]
	s_waitcnt lgkmcnt(9)
	v_mfma_f32_16x16x32_bf16 v[44:47], v[172:175], v[238:241], v[44:47]
	v_exp_f32_e32 v69, v69
	v_mfma_f32_16x16x32_bf16 v[40:43], v[172:175], v[216:219], v[40:43]
	v_exp_f32_e32 v66, v66
	ds_read_b128 v[172:175], v210 offset:51200
	v_mfma_f32_16x16x32_bf16 v[72:75], v[176:179], v[104:107], v[72:75]
	v_exp_f32_e32 v70, v70
	v_mfma_f32_16x16x32_bf16 v[76:79], v[176:179], v[120:123], v[76:79]
	v_exp_f32_e32 v67, v67
	ds_read_b128 v[176:179], v203 offset:8192
	s_waitcnt lgkmcnt(7)
	v_mfma_f32_16x16x32_bf16 v[48:51], v[180:183], v[216:219], v[48:51]
	v_exp_f32_e32 v71, v71
	v_mfma_f32_16x16x32_bf16 v[52:55], v[180:183], v[238:241], v[52:55]
	v_add_f32_e32 v220, v64, v65
	ds_read_b128 v[180:183], v210 offset:53248
	v_mfma_f32_16x16x32_bf16 v[76:79], v[230:233], v[124:127], v[76:79]
	v_add_f32_e32 v221, v68, v69
	v_mfma_f32_16x16x32_bf16 v[72:75], v[230:233], v[108:111], v[72:75]
	v_add_f32_e32 v220, v220, v66
	ds_read_b128 v[230:233], v246 offset:8192
	s_waitcnt lgkmcnt(6)
	v_mfma_f32_16x16x32_bf16 v[60:63], v[234:237], v[238:241], v[60:63]
	v_add_f32_e32 v221, v221, v70
	v_add_f32_e32 v220, v220, v67
	v_mfma_f32_16x16x32_bf16 v[56:59], v[234:237], v[216:219], v[56:59]
	v_add_f32_e32 v221, v221, v71
	ds_read_b128 v[234:237], v210 offset:55296
	v_mfma_f32_16x16x32_bf16 v[80:83], v[160:163], v[96:99], 0
	v_exp_f32_e32 v72, v72
	v_mfma_f32_16x16x32_bf16 v[84:87], v[160:163], v[112:115], 0
	v_exp_f32_e32 v76, v76
	ds_read_b128 v[160:163], v201 offset:12288
	s_waitcnt lgkmcnt(6)
	v_mfma_f32_16x16x32_bf16 v[0:3], v[164:167], v[242:245], v[0:3]
	v_exp_f32_e32 v73, v73
	v_mfma_f32_16x16x32_bf16 v[4:7], v[164:167], v[204:207], v[4:7]
	v_exp_f32_e32 v77, v77
	ds_read_b128 v[164:167], v210 offset:57344
	v_mfma_f32_16x16x32_bf16 v[84:87], v[168:171], v[116:119], v[84:87]
	v_exp_f32_e32 v74, v74
	v_mfma_f32_16x16x32_bf16 v[80:83], v[168:171], v[100:103], v[80:83]
	v_exp_f32_e32 v78, v78
	ds_read_b128 v[168:171], v202 offset:12288
	s_waitcnt lgkmcnt(6)
	v_mfma_f32_16x16x32_bf16 v[12:15], v[172:175], v[204:207], v[12:15]
	v_exp_f32_e32 v75, v75
	v_mfma_f32_16x16x32_bf16 v[8:11], v[172:175], v[242:245], v[8:11]
	v_exp_f32_e32 v79, v79
	ds_read_b128 v[172:175], v210 offset:59392
	v_mfma_f32_16x16x32_bf16 v[80:83], v[176:179], v[104:107], v[80:83]
	v_add_f32_e32 v220, v220, v72
	v_add_f32_e32 v221, v221, v76
	v_mfma_f32_16x16x32_bf16 v[84:87], v[176:179], v[120:123], v[84:87]
	v_add_f32_e32 v220, v220, v73
	ds_read_b128 v[176:179], v203 offset:12288
	s_add_u32 s10, s10, 0x200
	s_addc_u32 s11, s11, 0
	s_add_u32 s12, s12, 0x40000
	s_addc_u32 s13, s13, 0
	s_add_i32 s4, s4, 4
	s_cmpk_lt_u32 s4, 0x104
	s_cselect_b64 s[6:7], -1, 0
	s_and_b64 s[6:7], s[0:1], s[6:7]
	s_and_b64 vcc, exec, s[6:7]
	s_waitcnt lgkmcnt(6)
	v_mfma_f32_16x16x32_bf16 v[16:19], v[180:183], v[242:245], v[16:19]
	v_add_f32_e32 v221, v221, v77
	v_add_f32_e32 v220, v220, v74
	v_mfma_f32_16x16x32_bf16 v[20:23], v[180:183], v[204:207], v[20:23]
	v_add_f32_e32 v221, v221, v78
	ds_read_b128 v[180:183], v210 offset:61440
	v_mfma_f32_16x16x32_bf16 v[84:87], v[230:233], v[124:127], v[84:87]
	v_add_f32_e32 v220, v220, v75
	v_add_f32_e32 v221, v221, v79
	v_mfma_f32_16x16x32_bf16 v[80:83], v[230:233], v[108:111], v[80:83]
	v_cvt_pk_bf16_f32 v216, v64, v65
	ds_read_b128 v[230:233], v246 offset:12288
	s_waitcnt lgkmcnt(6)
	v_mfma_f32_16x16x32_bf16 v[28:31], v[234:237], v[204:207], v[28:31]
	v_cvt_pk_bf16_f32 v217, v66, v67
	v_cvt_pk_bf16_f32 v238, v68, v69
	v_mfma_f32_16x16x32_bf16 v[24:27], v[234:237], v[242:245], v[24:27]
	v_cvt_pk_bf16_f32 v239, v70, v71
	ds_read_b128 v[234:237], v210 offset:63488
	v_mfma_f32_16x16x32_bf16 v[88:91], v[160:163], v[96:99], 0
	v_exp_f32_e32 v80, v80
	v_mfma_f32_16x16x32_bf16 v[92:95], v[160:163], v[112:115], 0
	v_exp_f32_e32 v84, v84
	s_waitcnt lgkmcnt(5)
	v_mfma_f32_16x16x32_bf16 v[32:35], v[164:167], v[242:245], v[32:35]
	v_exp_f32_e32 v81, v81
	v_mfma_f32_16x16x32_bf16 v[36:39], v[164:167], v[204:207], v[36:39]
	v_exp_f32_e32 v85, v85
	v_mfma_f32_16x16x32_bf16 v[92:95], v[168:171], v[116:119], v[92:95]
	v_exp_f32_e32 v82, v82
	v_mfma_f32_16x16x32_bf16 v[88:91], v[168:171], v[100:103], v[88:91]
	v_exp_f32_e32 v86, v86
	s_waitcnt lgkmcnt(3)
	v_mfma_f32_16x16x32_bf16 v[44:47], v[172:175], v[204:207], v[44:47]
	v_exp_f32_e32 v83, v83
	v_mfma_f32_16x16x32_bf16 v[40:43], v[172:175], v[242:245], v[40:43]
	v_exp_f32_e32 v87, v87
	v_mfma_f32_16x16x32_bf16 v[88:91], v[176:179], v[104:107], v[88:91]
	v_add_f32_e32 v220, v220, v80
	v_add_f32_e32 v221, v221, v84
	v_mfma_f32_16x16x32_bf16 v[92:95], v[176:179], v[120:123], v[92:95]
	v_add_f32_e32 v220, v220, v81
	s_waitcnt lgkmcnt(0)
	s_barrier
	ds_read_b128 v[160:163], v201 offset:16384
	ds_read_b128 v[164:167], v209 offset:0
	ds_read_b128 v[168:171], v202 offset:16384
	ds_read_b128 v[172:175], v209 offset:2048
	ds_read_b128 v[176:179], v203 offset:16384
	v_mfma_f32_16x16x32_bf16 v[48:51], v[180:183], v[242:245], v[48:51]
	v_add_f32_e32 v221, v221, v85
	v_add_f32_e32 v220, v220, v82
	v_mfma_f32_16x16x32_bf16 v[52:55], v[180:183], v[204:207], v[52:55]
	v_add_f32_e32 v221, v221, v86
	ds_read_b128 v[180:183], v209 offset:4096
	v_mfma_f32_16x16x32_bf16 v[92:95], v[230:233], v[124:127], v[92:95]
	v_add_f32_e32 v220, v220, v83
	v_add_f32_e32 v221, v221, v87
	v_mfma_f32_16x16x32_bf16 v[88:91], v[230:233], v[108:111], v[88:91]
	v_cvt_pk_bf16_f32 v218, v72, v73
	ds_read_b128 v[230:233], v246 offset:16384
	s_waitcnt lgkmcnt(6)
	v_mfma_f32_16x16x32_bf16 v[60:63], v[234:237], v[204:207], v[60:63]
	v_cvt_pk_bf16_f32 v219, v74, v75
	v_cvt_pk_bf16_f32 v240, v76, v77
	v_mfma_f32_16x16x32_bf16 v[56:59], v[234:237], v[242:245], v[56:59]
	v_cvt_pk_bf16_f32 v241, v78, v79
	ds_read_b128 v[234:237], v209 offset:6144
	s_cbranch_vccnz .LBB0_734
	s_setprio 0
	s_waitcnt vmcnt(0)
	s_nop 7
	s_nop 7
	ds_swizzle_b32 v64, v194 offset:swizzle(SWAP,16)
	s_waitcnt lgkmcnt(0)
	v_add_f32_e32 v194, v194, v64
	v_mov_b32_e32 v65, v194
	s_nop 1
	v_permlane32_swap_b32_e32 v194, v65
	v_add_f32_e32 v194, v194, v65
	s_nop 0
	v_rcp_f32_e32 v66, v194
	ds_swizzle_b32 v64, v195 offset:swizzle(SWAP,16)
	s_waitcnt lgkmcnt(0)
	v_add_f32_e32 v195, v195, v64
	v_mov_b32_e32 v65, v195
	s_nop 1
	v_permlane32_swap_b32_e32 v195, v65
	v_add_f32_e32 v195, v195, v65
	s_nop 0
	v_rcp_f32_e32 v67, v195
	v_readlane_b32 s100, v250, 8
	v_mbcnt_lo_u32_b32 v68, -1, 0
	v_mbcnt_hi_u32_b32 v68, -1, v68
	v_and_b32_e32 v69, 15, v68
	v_lshrrev_b32_e32 v70, 4, v68
	s_lshr_b32 s101, s100, 1
	v_add_u32_e32 v69, s101, v69
	v_lshlrev_b32_e32 v69, 12, v69
	v_and_b32_e32 v71, 1, v70
	v_lshlrev_b32_e32 v71, 5, v71
	v_and_b32_e32 v70, 2, v70
	v_lshl_add_u32 v71, v70, 3, v71
	v_add_u32_e32 v70, v69, v71
	v_add_u32_e32 v71, 0x10000, v70
	v_mul_f32_e32 v0, v0, v66
	v_mul_f32_e32 v1, v1, v66
	v_mul_f32_e32 v2, v2, v66
	v_mul_f32_e32 v3, v3, v66
	v_mul_f32_e32 v8, v8, v66
	v_mul_f32_e32 v9, v9, v66
	v_mul_f32_e32 v10, v10, v66
	v_mul_f32_e32 v11, v11, v66
	v_cvt_pk_bf16_f32 v72, v0, v1
	v_cvt_pk_bf16_f32 v73, v2, v3
	v_cvt_pk_bf16_f32 v74, v8, v9
	v_cvt_pk_bf16_f32 v75, v10, v11
	s_nop 1
	v_permlane16_swap_b32_e32 v72, v74
	v_permlane16_swap_b32_e32 v73, v75
	s_nop 1
	global_store_dwordx4 v70, v[72:75], s[58:59] offset:0
	v_mul_f32_e32 v16, v16, v66
	v_mul_f32_e32 v17, v17, v66
	v_mul_f32_e32 v18, v18, v66
	v_mul_f32_e32 v19, v19, v66
	v_mul_f32_e32 v24, v24, v66
	v_mul_f32_e32 v25, v25, v66
	v_mul_f32_e32 v26, v26, v66
	v_mul_f32_e32 v27, v27, v66
	v_cvt_pk_bf16_f32 v76, v16, v17
	v_cvt_pk_bf16_f32 v77, v18, v19
	v_cvt_pk_bf16_f32 v78, v24, v25
	v_cvt_pk_bf16_f32 v79, v26, v27
	s_nop 1
	v_permlane16_swap_b32_e32 v76, v78
	v_permlane16_swap_b32_e32 v77, v79
	s_nop 1
	global_store_dwordx4 v70, v[76:79], s[58:59] offset:64
	v_mul_f32_e32 v32, v32, v66
	v_mul_f32_e32 v33, v33, v66
	v_mul_f32_e32 v34, v34, v66
	v_mul_f32_e32 v35, v35, v66
	v_mul_f32_e32 v40, v40, v66
	v_mul_f32_e32 v41, v41, v66
	v_mul_f32_e32 v42, v42, v66
	v_mul_f32_e32 v43, v43, v66
	v_cvt_pk_bf16_f32 v80, v32, v33
	v_cvt_pk_bf16_f32 v81, v34, v35
	v_cvt_pk_bf16_f32 v82, v40, v41
	v_cvt_pk_bf16_f32 v83, v42, v43
	s_nop 1
	v_permlane16_swap_b32_e32 v80, v82
	v_permlane16_swap_b32_e32 v81, v83
	s_nop 1
	global_store_dwordx4 v70, v[80:83], s[58:59] offset:128
	v_mul_f32_e32 v48, v48, v66
	v_mul_f32_e32 v49, v49, v66
	v_mul_f32_e32 v50, v50, v66
	v_mul_f32_e32 v51, v51, v66
	v_mul_f32_e32 v56, v56, v66
	v_mul_f32_e32 v57, v57, v66
	v_mul_f32_e32 v58, v58, v66
	v_mul_f32_e32 v59, v59, v66
	v_cvt_pk_bf16_f32 v84, v48, v49
	v_cvt_pk_bf16_f32 v85, v50, v51
	v_cvt_pk_bf16_f32 v86, v56, v57
	v_cvt_pk_bf16_f32 v87, v58, v59
	s_nop 1
	v_permlane16_swap_b32_e32 v84, v86
	v_permlane16_swap_b32_e32 v85, v87
	s_nop 1
	global_store_dwordx4 v70, v[84:87], s[58:59] offset:192
	v_mul_f32_e32 v4, v4, v67
	v_mul_f32_e32 v5, v5, v67
	v_mul_f32_e32 v6, v6, v67
	v_mul_f32_e32 v7, v7, v67
	v_mul_f32_e32 v12, v12, v67
	v_mul_f32_e32 v13, v13, v67
	v_mul_f32_e32 v14, v14, v67
	v_mul_f32_e32 v15, v15, v67
	v_cvt_pk_bf16_f32 v88, v4, v5
	v_cvt_pk_bf16_f32 v89, v6, v7
	v_cvt_pk_bf16_f32 v90, v12, v13
	v_cvt_pk_bf16_f32 v91, v14, v15
	s_nop 1
	v_permlane16_swap_b32_e32 v88, v90
	v_permlane16_swap_b32_e32 v89, v91
	s_nop 1
	global_store_dwordx4 v71, v[88:91], s[58:59] offset:0
	v_mul_f32_e32 v20, v20, v67
	v_mul_f32_e32 v21, v21, v67
	v_mul_f32_e32 v22, v22, v67
	v_mul_f32_e32 v23, v23, v67
	v_mul_f32_e32 v28, v28, v67
	v_mul_f32_e32 v29, v29, v67
	v_mul_f32_e32 v30, v30, v67
	v_mul_f32_e32 v31, v31, v67
	v_cvt_pk_bf16_f32 v92, v20, v21
	v_cvt_pk_bf16_f32 v93, v22, v23
	v_cvt_pk_bf16_f32 v94, v28, v29
	v_cvt_pk_bf16_f32 v95, v30, v31
	s_nop 1
	v_permlane16_swap_b32_e32 v92, v94
	v_permlane16_swap_b32_e32 v93, v95
	s_nop 1
	global_store_dwordx4 v71, v[92:95], s[58:59] offset:64
	v_mul_f32_e32 v36, v36, v67
	v_mul_f32_e32 v37, v37, v67
	v_mul_f32_e32 v38, v38, v67
	v_mul_f32_e32 v39, v39, v67
	v_mul_f32_e32 v44, v44, v67
	v_mul_f32_e32 v45, v45, v67
	v_mul_f32_e32 v46, v46, v67
	v_mul_f32_e32 v47, v47, v67
	v_cvt_pk_bf16_f32 v72, v36, v37
	v_cvt_pk_bf16_f32 v73, v38, v39
	v_cvt_pk_bf16_f32 v74, v44, v45
	v_cvt_pk_bf16_f32 v75, v46, v47
	s_nop 1
	v_permlane16_swap_b32_e32 v72, v74
	v_permlane16_swap_b32_e32 v73, v75
	s_nop 1
	global_store_dwordx4 v71, v[72:75], s[58:59] offset:128
	v_mul_f32_e32 v52, v52, v67
	v_mul_f32_e32 v53, v53, v67
	v_mul_f32_e32 v54, v54, v67
	v_mul_f32_e32 v55, v55, v67
	v_mul_f32_e32 v60, v60, v67
	v_mul_f32_e32 v61, v61, v67
	v_mul_f32_e32 v62, v62, v67
	v_mul_f32_e32 v63, v63, v67
	v_cvt_pk_bf16_f32 v76, v52, v53
	v_cvt_pk_bf16_f32 v77, v54, v55
	v_cvt_pk_bf16_f32 v78, v60, v61
	v_cvt_pk_bf16_f32 v79, v62, v63
	s_nop 1
	v_permlane16_swap_b32_e32 v76, v78
	v_permlane16_swap_b32_e32 v77, v79
	s_nop 1
	global_store_dwordx4 v71, v[76:79], s[58:59] offset:192
	s_barrier
